# DeltaNet scan: nt on the LDS-DMA fragment loads (each fragment is read once per workgroup)
# speedup vs baseline: 1.0057x; 1.0057x over previous
.LBB0_681:
	v_and_b32_e32 v67, 63, v66
	s_mul_i32 s17, s14, 0x2400
	v_lshlrev_b32_e32 v130, 4, v67
	s_add_i32 m0, s17, 0
	v_cndmask_b32_e64 v3, 0, 1, s[0:1]
	global_load_lds_dwordx4 v130, s[2:3] nt
	s_add_i32 s18, s16, 1
	v_cmp_ne_u32_e64 s[2:3], 1, v3
	s_andn2_b64 vcc, exec, s[0:1]
	s_mov_b64 s[6:7], -1
	s_cbranch_vccnz .LBB0_683
	s_sub_i32 s4, s16, 55
	s_lshr_b32 s4, s4, 3
	s_add_i32 s4, s4, s44
	s_mov_b32 s5, s79
	s_lshl_b32 s4, s4, 11
	s_lshl_b64 s[4:5], s[4:5], 2
	s_add_u32 s4, s15, s4
	s_addc_u32 s5, s42, s5
	s_lshl_b32 s6, s18, 10
	s_and_b32 s6, s6, 0x1c00
	s_add_u32 s4, s4, s6
	s_addc_u32 s5, s5, 0
	s_mov_b64 s[6:7], 0

.LBB0_685:
	s_lshl_b32 s19, s18, 10
	v_lshl_add_u64 v[4:5], s[4:5], 0, v[130:131]
	s_add_i32 m0, s19, 0
	s_add_i32 s20, s16, 2
	global_load_lds_dwordx4 v[4:5], off nt
	s_cmp_gt_i32 s14, 5
	s_cselect_b64 s[6:7], -1, 0
	s_cmp_lt_i32 s14, 6
	s_mov_b64 s[8:9], -1
	s_cbranch_scc1 .LBB0_687
	s_sub_i32 s4, s16, 54
	s_lshr_b32 s4, s4, 3
	s_add_i32 s4, s4, s44
	s_mov_b32 s5, s79
	s_lshl_b32 s4, s4, 11
	s_lshl_b64 s[4:5], s[4:5], 2
	s_add_u32 s4, s15, s4
	s_addc_u32 s5, s42, s5
	s_lshl_b32 s8, s20, 10
	s_and_b32 s8, s8, 0x1c00
	s_add_u32 s4, s4, s8
	s_addc_u32 s5, s5, 0
	s_mov_b64 s[8:9], 0

.LBB0_689:
	s_lshl_b32 s21, s20, 10
	v_lshl_add_u64 v[4:5], s[4:5], 0, v[130:131]
	s_add_i32 m0, s21, 0
	v_cndmask_b32_e64 v3, 0, 1, s[6:7]
	global_load_lds_dwordx4 v[4:5], off nt
	s_add_i32 s22, s16, 3
	v_cmp_ne_u32_e64 s[4:5], 1, v3
	s_andn2_b64 vcc, exec, s[6:7]
	s_mov_b64 s[8:9], -1
	s_cbranch_vccnz .LBB0_691
	s_sub_i32 s6, s16, 53
	s_lshr_b32 s6, s6, 3
	s_add_i32 s6, s6, s44
	s_mov_b32 s7, s79
	s_lshl_b32 s6, s6, 11
	s_lshl_b64 s[6:7], s[6:7], 2
	s_add_u32 s6, s15, s6
	s_addc_u32 s7, s42, s7
	s_lshl_b32 s8, s22, 10
	s_and_b32 s8, s8, 0x1c00
	s_add_u32 s6, s6, s8
	s_addc_u32 s7, s7, 0
	s_mov_b64 s[8:9], 0

.LBB0_693:
	s_lshl_b32 s23, s22, 10
	v_lshl_add_u64 v[4:5], s[6:7], 0, v[130:131]
	s_add_i32 m0, s23, 0
	s_add_i32 s24, s16, 4
	global_load_lds_dwordx4 v[4:5], off nt
	s_and_b64 vcc, exec, s[4:5]
	s_mov_b64 s[8:9], -1
	s_cbranch_vccnz .LBB0_695
	s_sub_i32 s6, s16, 52
	s_lshr_b32 s6, s6, 3
	s_add_i32 s6, s6, s44
	s_mov_b32 s7, s79
	s_lshl_b32 s6, s6, 11
	s_lshl_b64 s[6:7], s[6:7], 2
	s_add_u32 s6, s15, s6
	s_addc_u32 s7, s42, s7
	s_lshl_b32 s8, s24, 10
	s_and_b32 s8, s8, 0x1c00
	s_add_u32 s6, s6, s8
	s_addc_u32 s7, s7, 0
	s_mov_b64 s[8:9], 0

.LBB0_697:
	s_lshl_b32 s25, s24, 10
	v_lshl_add_u64 v[4:5], s[6:7], 0, v[130:131]
	s_add_i32 m0, s25, 0
	s_add_i32 s26, s16, 5
	global_load_lds_dwordx4 v[4:5], off nt
	s_and_b64 vcc, exec, s[4:5]
	s_mov_b64 s[8:9], -1
	s_cbranch_vccnz .LBB0_699
	s_sub_i32 s6, s16, 51
	s_lshr_b32 s6, s6, 3
	s_add_i32 s6, s6, s44
	s_mov_b32 s7, s79
	s_lshl_b32 s6, s6, 11
	s_lshl_b64 s[6:7], s[6:7], 2
	s_add_u32 s6, s15, s6
	s_addc_u32 s7, s42, s7
	s_lshl_b32 s8, s26, 10
	s_and_b32 s8, s8, 0x1c00
	s_add_u32 s6, s6, s8
	s_addc_u32 s7, s7, 0
	s_mov_b64 s[8:9], 0

.LBB0_701:
	s_lshl_b32 s27, s26, 10
	v_lshl_add_u64 v[4:5], s[6:7], 0, v[130:131]
	s_add_i32 m0, s27, 0
	s_add_i32 s28, s16, 6
	global_load_lds_dwordx4 v[4:5], off nt
	s_and_b64 vcc, exec, s[4:5]
	s_mov_b64 s[8:9], -1
	s_cbranch_vccnz .LBB0_703
	s_sub_i32 s6, s16, 50
	s_lshr_b32 s6, s6, 3
	s_add_i32 s6, s6, s44
	s_mov_b32 s7, s79
	s_lshl_b32 s6, s6, 11
	s_lshl_b64 s[6:7], s[6:7], 2
	s_add_u32 s6, s15, s6
	s_addc_u32 s7, s42, s7
	s_lshl_b32 s8, s28, 10
	s_and_b32 s8, s8, 0x1c00
	s_add_u32 s6, s6, s8
	s_addc_u32 s7, s7, 0
	s_mov_b64 s[8:9], 0

.LBB0_705:
	s_lshl_b32 s29, s28, 10
	v_lshl_add_u64 v[4:5], s[6:7], 0, v[130:131]
	s_add_i32 m0, s29, 0
	s_add_i32 s30, s16, 7
	global_load_lds_dwordx4 v[4:5], off nt
	s_and_b64 vcc, exec, s[4:5]
	s_mov_b64 s[8:9], -1
	s_cbranch_vccnz .LBB0_707
	s_sub_i32 s6, s16, 49
	s_lshr_b32 s6, s6, 3
	s_add_i32 s6, s6, s44
	s_mov_b32 s7, s79
	s_lshl_b32 s6, s6, 11
	s_lshl_b64 s[6:7], s[6:7], 2
	s_add_u32 s6, s15, s6
	s_addc_u32 s7, s42, s7
	s_lshl_b32 s8, s30, 10
	s_and_b32 s8, s8, 0x1c00
	s_add_u32 s6, s6, s8
	s_addc_u32 s7, s7, 0
	s_mov_b64 s[8:9], 0

.LBB0_709:
	s_lshl_b32 s31, s30, 10
	v_lshl_add_u64 v[4:5], s[6:7], 0, v[130:131]
	s_add_i32 m0, s31, 0
	s_add_i32 s36, s16, 8
	global_load_lds_dwordx4 v[4:5], off nt
	s_and_b64 vcc, exec, s[4:5]
	s_mov_b64 s[12:13], -1
	s_cbranch_vccnz .LBB0_711
	s_sub_i32 s6, s16, 48
	s_lshr_b32 s6, s6, 3
	s_add_i32 s6, s6, s44
	s_mov_b32 s47, s79
	s_lshl_b32 s46, s6, 11
	s_lshl_b64 s[6:7], s[46:47], 2
	s_add_u32 s6, s15, s6
	s_addc_u32 s7, s42, s7
	s_lshl_b32 s8, s14, 8
	s_and_b32 s10, s8, 0x700
	s_lshl_b32 s8, s10, 2
	s_add_u32 s6, s6, s8
	s_mov_b32 s11, s79
	s_addc_u32 s7, s7, 0
	s_mov_b32 s37, s79
	s_mov_b64 s[12:13], 0
	s_mov_b64 s[8:9], s[46:47]

.LBB0_713:
	v_lshl_add_u64 v[68:69], s[6:7], 0, v[130:131]
	v_readlane_b32 s6, v252, 44
	v_readlane_b32 s7, v252, 45
	s_lshl_b32 s48, s36, 10
	s_add_i32 m0, s48, 0
	s_and_b32 s12, s14, 1
	global_load_lds_dwordx4 v[68:69], off nt
	s_nop 0
	global_load_dword v134, v131, s[6:7]
	s_or_b32 s74, s12, s44
	s_cmp_lt_i32 s14, 2
	s_cselect_b64 s[6:7], -1, 0
	s_sub_i32 s52, s16, 51
	s_lshr_b32 s52, s52, 3
	s_add_i32 s52, s52, s44
	s_sub_i32 s12, s16, 56
	s_lshl_b32 s68, s52, 11
	s_sub_i32 s52, s16, 50
	s_lshr_b32 s12, s12, 3
	s_lshr_b32 s52, s52, 3
	s_add_i32 s12, s12, s44
	s_add_i32 s52, s52, s44
	s_lshl_b32 s49, s14, 13
	s_lshl_b32 s40, s12, 11
	s_sub_i32 s12, s16, 55
	s_sub_i32 s14, s16, 54
	s_sub_i32 s42, s16, 53
	s_sub_i32 s46, s16, 52
	s_lshl_b32 s70, s52, 11
	s_sub_i32 s52, s16, 49
	s_lshr_b32 s12, s12, 3
	s_lshr_b32 s14, s14, 3
	s_lshr_b32 s42, s42, 3
	s_lshr_b32 s46, s46, 3
	s_lshr_b32 s52, s52, 3
	s_mov_b32 s41, s79
	s_add_i32 s12, s12, s44
	s_add_i32 s14, s14, s44
	s_add_i32 s42, s42, s44
	s_add_i32 s46, s46, s44
	s_add_i32 s52, s52, s44
	s_ashr_i32 s50, s16, 31
	s_lshl_b32 s12, s12, 11
	s_ashr_i32 s51, s18, 31
	s_lshl_b32 s14, s14, 11
	s_ashr_i32 s53, s20, 31
	s_lshl_b32 s42, s42, 11
	s_ashr_i32 s54, s22, 31
	s_lshl_b32 s46, s46, 11
	s_ashr_i32 s55, s24, 31
	s_ashr_i32 s56, s26, 31
	s_ashr_i32 s57, s28, 31
	s_lshl_b32 s72, s52, 11
	s_ashr_i32 s58, s30, 31
	s_lshl_b64 s[60:61], s[40:41], 2
	v_readlane_b32 s44, v252, 38
	s_add_u32 s52, s44, s60
	v_readlane_b32 s45, v252, 40
	s_addc_u32 s60, s45, s61
	s_lshl_b64 s[10:11], s[10:11], 2
	s_mov_b32 s13, s79
	s_add_u32 s59, s52, s10
	s_addc_u32 s60, s60, s11
	s_lshl_b64 s[12:13], s[12:13], 2
	s_add_u32 s12, s44, s12
	s_addc_u32 s13, s45, s13
	s_and_b32 s52, s19, 0x1c00
	s_mov_b32 s15, s79
	s_add_u32 s61, s12, s52
	s_addc_u32 s62, s13, 0
	s_lshl_b64 s[12:13], s[14:15], 2
	s_add_u32 s12, s44, s12
	s_addc_u32 s13, s45, s13
	s_and_b32 s14, s21, 0x1c00
	s_mov_b32 s43, s79
	s_add_u32 s63, s12, s14
	s_addc_u32 s64, s13, 0
	s_lshl_b64 s[12:13], s[42:43], 2
	s_add_u32 s12, s44, s12
	s_addc_u32 s13, s45, s13
	s_and_b32 s14, s23, 0x1c00
	s_mov_b32 s47, s79
	s_add_u32 s65, s12, s14
	s_addc_u32 s66, s13, 0
	s_lshl_b64 s[12:13], s[46:47], 2
	s_add_u32 s12, s44, s12
	s_addc_u32 s13, s45, s13
	s_and_b32 s14, s25, 0x1c00
	s_mov_b32 s69, s79
	s_add_u32 s67, s12, s14
	s_addc_u32 s86, s13, 0
	s_lshl_b64 s[12:13], s[68:69], 2
	s_add_u32 s12, s44, s12
	s_addc_u32 s13, s45, s13
	s_and_b32 s14, s27, 0x1c00
	s_mov_b32 s71, s79
	s_add_u32 s87, s12, s14
	s_addc_u32 s94, s13, 0
	s_lshl_b64 s[12:13], s[70:71], 2
	s_add_u32 s12, s44, s12
	s_addc_u32 s13, s45, s13
	s_and_b32 s14, s29, 0x1c00
	s_mov_b32 s73, s79
	s_add_u32 s95, s12, s14
	s_addc_u32 s96, s13, 0
	s_lshl_b64 s[12:13], s[72:73], 2
	s_add_u32 s12, s44, s12
	s_addc_u32 s13, s45, s13
	s_and_b32 s14, s31, 0x1c00
	s_add_u32 s97, s12, s14
	s_addc_u32 s42, s13, 0
	s_lshl_b64 s[8:9], s[8:9], 2
	s_add_u32 s8, s44, s8
	s_addc_u32 s9, s45, s9
	s_add_u32 s43, s8, s10
	s_addc_u32 s52, s9, s11
	s_lshl_b32 s8, s74, 6
	v_readlane_b32 s9, v252, 52
	v_and_b32_e32 v66, 31, v66
	s_add_u32 s8, s9, s8
	v_readlane_b32 s9, v252, 55
	v_lshrrev_b32_e32 v135, 5, v67
	v_readlane_b32 s40, v252, 16
	s_addc_u32 s9, s9, 0
	v_lshlrev_b32_e32 v66, 1, v66
	v_mov_b32_e32 v67, v131
	v_readlane_b32 s72, v252, 50
	v_mov_b32_e32 v3, v2
	v_mov_b32_e32 v4, v2
	v_mov_b32_e32 v5, v2
	v_mov_b32_e32 v6, v2
	v_mov_b32_e32 v7, v2
	v_mov_b32_e32 v8, v2
	v_mov_b32_e32 v9, v2
	v_mov_b32_e32 v10, v2
	v_mov_b32_e32 v11, v2
	v_mov_b32_e32 v12, v2
	v_mov_b32_e32 v13, v2
	v_mov_b32_e32 v14, v2
	v_mov_b32_e32 v15, v2
	v_mov_b32_e32 v16, v2
	v_mov_b32_e32 v17, v2
	v_mov_b32_e32 v19, v18
	v_mov_b32_e32 v20, v18
	v_mov_b32_e32 v21, v18
	v_mov_b32_e32 v22, v18
	v_mov_b32_e32 v23, v18
	v_mov_b32_e32 v24, v18
	v_mov_b32_e32 v25, v18
	v_mov_b32_e32 v26, v18
	v_mov_b32_e32 v27, v18
	v_mov_b32_e32 v28, v18
	v_mov_b32_e32 v29, v18
	v_mov_b32_e32 v30, v18
	v_mov_b32_e32 v31, v18
	v_mov_b32_e32 v32, v18
	v_mov_b32_e32 v33, v18
	v_mov_b32_e32 v35, v34
	v_mov_b32_e32 v36, v34
	v_mov_b32_e32 v37, v34
	v_mov_b32_e32 v38, v34
	v_mov_b32_e32 v39, v34
	v_mov_b32_e32 v40, v34
	v_mov_b32_e32 v41, v34
	v_mov_b32_e32 v42, v34
	v_mov_b32_e32 v43, v34
	v_mov_b32_e32 v44, v34
	v_mov_b32_e32 v45, v34
	v_mov_b32_e32 v46, v34
	v_mov_b32_e32 v47, v34
	v_mov_b32_e32 v48, v34
	v_mov_b32_e32 v49, v34
	v_mov_b32_e32 v51, v50
	v_mov_b32_e32 v52, v50
	v_mov_b32_e32 v53, v50
	v_mov_b32_e32 v54, v50
	v_mov_b32_e32 v55, v50
	v_mov_b32_e32 v56, v50
	v_mov_b32_e32 v57, v50
	v_mov_b32_e32 v58, v50
	v_mov_b32_e32 v59, v50
	v_mov_b32_e32 v60, v50
	v_mov_b32_e32 v61, v50
	v_mov_b32_e32 v62, v50
	v_mov_b32_e32 v63, v50
	v_mov_b32_e32 v64, v50
	v_mov_b32_e32 v65, v50
	v_add_u32_e32 v136, 0, v130
	v_readlane_b32 s41, v252, 17
	v_lshl_add_u64 v[132:133], s[8:9], 0, v[66:67]
	s_mov_b32 s46, 34
	s_mov_b32 s47, -4
	s_waitcnt vmcnt(0)
	v_mov_b32_e32 v137, v134
	v_readlane_b32 s44, v252, 37
	v_readlane_b32 s73, v252, 51
	v_readlane_b32 s45, v252, 46
	v_readlane_b32 s71, v252, 47
	v_readlane_b32 s74, v252, 48
	s_lshl_b32 s10, s16, 10
	s_add_u32 s10, s40, s10
	s_addc_u32 s11, s41, 0
	s_cmp_lg_u64 s[0:1], 0
	s_cselect_b32 s59, s59, s10
	s_cselect_b32 s60, s60, s11
	s_lshl_b32 s10, s18, 10
	s_add_u32 s10, s40, s10
	s_addc_u32 s11, s41, 0
	s_cmp_lg_u64 s[0:1], 0
	s_cselect_b32 s61, s61, s10
	s_cselect_b32 s62, s62, s11
	s_lshl_b32 s10, s20, 10
	s_add_u32 s10, s40, s10
	s_addc_u32 s11, s41, 0
	s_cmp_eq_u64 s[4:5], 0
	s_cselect_b32 s63, s63, s10
	s_cselect_b32 s64, s64, s11
	s_lshl_b32 s10, s22, 10
	s_add_u32 s10, s40, s10
	s_addc_u32 s11, s41, 0
	s_cmp_eq_u64 s[4:5], 0
	s_cselect_b32 s65, s65, s10
	s_cselect_b32 s66, s66, s11
	s_lshl_b32 s10, s24, 10
	s_add_u32 s10, s40, s10
	s_addc_u32 s11, s41, 0
	s_cmp_eq_u64 s[4:5], 0
	s_cselect_b32 s67, s67, s10
	s_cselect_b32 s86, s86, s11
	s_lshl_b32 s10, s26, 10
	s_add_u32 s10, s40, s10
	s_addc_u32 s11, s41, 0
	s_cmp_eq_u64 s[4:5], 0
	s_cselect_b32 s87, s87, s10
	s_cselect_b32 s94, s94, s11
	s_lshl_b32 s10, s28, 10
	s_add_u32 s10, s40, s10
	s_addc_u32 s11, s41, 0
	s_cmp_eq_u64 s[4:5], 0
	s_cselect_b32 s95, s95, s10
	s_cselect_b32 s96, s96, s11
	s_lshl_b32 s10, s30, 10
	s_add_u32 s10, s40, s10
	s_addc_u32 s11, s41, 0
	s_cmp_eq_u64 s[4:5], 0
	s_cselect_b32 s97, s97, s10
	s_cselect_b32 s42, s42, s11
	s_lshl_b32 s10, s36, 10
	s_add_u32 s10, s40, s10
	s_addc_u32 s11, s41, 0
	s_cmp_eq_u64 s[4:5], 0
	s_cselect_b32 s43, s43, s10
	s_cselect_b32 s52, s52, s11
	v_readfirstlane_b32 s2, v0
	s_nop 0
	s_lshr_b32 s2, s2, 8
	s_cmp_lg_u32 s2, 0
	s_cselect_b64 s[2:3], -1, 0
	s_branch .LBB0_716

.LBB0_728:
	s_lshl_b32 s8, s10, 3
	s_add_i32 s12, s8, s45
	s_ashr_i32 s13, s12, 31
	s_lshl_b64 s[8:9], s[12:13], 15
	s_mul_i32 s14, s12, 0xe000
	s_bitcmp1_b32 s70, 0
	s_cselect_b32 s15, 0x12000, 0
	s_cmp_lg_u64 s[0:1], 0
	s_cselect_b32 s13, s8, s14
	s_cmp_lg_u64 s[4:5], 0
	s_cselect_b32 s69, s14, s8
	s_add_u32 s10, s59, s13
	s_addc_u32 s11, s60, 0
	s_add_i32 m0, s15, s17
	v_lshl_add_u64 v[66:67], s[10:11], 0, v[130:131]
	global_load_lds_dwordx4 v[66:67], off nt
	s_add_u32 s10, s61, s13
	s_addc_u32 s11, s62, 0
	s_add_i32 m0, s15, s19
	v_lshl_add_u64 v[66:67], s[10:11], 0, v[130:131]
	global_load_lds_dwordx4 v[66:67], off nt
	s_add_u32 s10, s63, s69
	s_addc_u32 s11, s64, 0
	s_add_i32 m0, s15, s21
	v_lshl_add_u64 v[66:67], s[10:11], 0, v[130:131]
	global_load_lds_dwordx4 v[66:67], off nt
	s_add_u32 s10, s65, s69
	s_addc_u32 s11, s66, 0
	s_add_i32 m0, s15, s23
	v_lshl_add_u64 v[66:67], s[10:11], 0, v[130:131]
	global_load_lds_dwordx4 v[66:67], off nt
	s_add_u32 s10, s67, s69
	s_addc_u32 s11, s86, 0
	s_add_i32 m0, s15, s25
	v_lshl_add_u64 v[66:67], s[10:11], 0, v[130:131]
	global_load_lds_dwordx4 v[66:67], off nt
	s_add_u32 s10, s87, s69
	s_addc_u32 s11, s94, 0
	s_add_i32 m0, s15, s27
	v_lshl_add_u64 v[66:67], s[10:11], 0, v[130:131]
	global_load_lds_dwordx4 v[66:67], off nt
	s_add_u32 s10, s95, s69
	s_addc_u32 s11, s96, 0
	s_add_i32 m0, s15, s29
	v_lshl_add_u64 v[66:67], s[10:11], 0, v[130:131]
	global_load_lds_dwordx4 v[66:67], off nt
	s_add_u32 s10, s97, s69
	s_addc_u32 s11, s42, 0
	s_add_i32 m0, s15, s31
	v_lshl_add_u64 v[66:67], s[10:11], 0, v[130:131]
	global_load_lds_dwordx4 v[66:67], off nt
	s_add_u32 s10, s43, s69
	s_addc_u32 s11, s52, 0
	s_add_i32 m0, s15, s48
	v_lshl_add_u64 v[66:67], s[10:11], 0, v[130:131]
	global_load_lds_dwordx4 v[66:67], off nt
	s_andn2_b64 vcc, exec, s[6:7]
	s_cbranch_vccnz .Lscan_w2
